# barrier: XCD leader issues its L1 invalidate before the L2 write-back (overlapped), rest as compact-poll version
# baseline (speedup 1.0000x reference)
; __device__ __forceinline__ unsigned xb_ld(unsigned* p)              { return __hip_atomic_load(p, __ATOMIC_RELAXED, __HIP_MEMORY_SCOPE_AGENT); }
; __device__ __forceinline__ unsigned xb_add(unsigned* p, unsigned v) { return __hip_atomic_fetch_add(p, v, __ATOMIC_RELAXED, __HIP_MEMORY_SCOPE_AGENT); }
; #define XB_SPIN(cond, bar) do { unsigned _sp = 0; while (cond) { __builtin_amdgcn_s_sleep(1); \
;     if ((++_sp & 255u) == 0u) { if (xb_ld(&(bar)[XB_TMO])) break; if (_sp > XB_SPIN_CAP) { atomicAdd(&(bar)[XB_TMO], 1u); break; } } } } while (0)
; __device__ __forceinline__ void xcd_barrier(const XcdBarrier& b) {
;     ...
;         unsigned nloc = b.st[0], nx = b.st[1];
;         if (nloc == 0u) { xcd_barrier_complete(bar, b.x, nloc, nx); b.st[0] = nloc; b.st[1] = nx; }
;         const unsigned old = xb_add(&bar[XB_XSUB(b.x)], one_);
;         const unsigned gen = old / nloc;
;         if (old + 1u == (gen + 1u) * nloc) {
;             __builtin_amdgcn_fence(__ATOMIC_RELEASE, "agent");
;             asm volatile("s_waitcnt vmcnt(0)" ::: "memory");
;             const unsigned og = xb_add(&bar[XB_TOP], one_);
;             const unsigned tg = og / nx;
;             if (og + 1u == (tg + 1u) * nx) xb_add(&bar[XB_TOPGEN], one_);
;             else XB_SPIN(xb_ld(&bar[XB_TOPGEN]) == tg, bar);
;             __builtin_amdgcn_fence(__ATOMIC_ACQUIRE, "agent");
;             xb_add(&bar[XB_XGEN(b.x)], one_);
;             asm volatile("s_waitcnt vmcnt(0)" ::: "memory");
;         } else {
;             XB_SPIN(xb_ld(&bar[XB_XGEN(b.x)]) == gen, bar);
;             __builtin_amdgcn_fence(__ATOMIC_ACQUIRE, "agent");
;             asm volatile("s_waitcnt vmcnt(0)" ::: "memory");
;         }
.LBB0_142:
	s_lshl_b32 s2, s33, 8
	s_add_u32 s23, s34, s2
	s_addc_u32 s22, s35, 0
	v_mov_b32_e32 v1, s23
	v_add_co_u32_e32 v4, vcc, 0x1000, v1
	v_mov_b32_e32 v1, s22
	s_nop 0
	v_addc_co_u32_e32 v5, vcc, 0, v1, vcc
	flat_atomic_add v1, v[4:5], v10 offset:1024 sc0
	v_cvt_f32_u32_e32 v3, v2
	v_sub_u32_e32 v4, 0, v2
	v_rcp_iflag_f32_e32 v3, v3
	s_nop 0
	v_mul_f32_e32 v3, 0x4f7ffffe, v3
	v_cvt_u32_f32_e32 v3, v3
	v_mul_lo_u32 v4, v4, v3
	v_mul_hi_u32 v4, v3, v4
	v_add_u32_e32 v3, v3, v4
	s_waitcnt vmcnt(0) lgkmcnt(0)
	v_mul_hi_u32 v3, v1, v3
	v_mul_lo_u32 v5, v3, v2
	v_add_u32_e32 v4, 1, v1
	v_sub_u32_e32 v1, v1, v5
	v_add_u32_e32 v6, 1, v3
	v_cmp_ge_u32_e32 vcc, v1, v2
	v_sub_u32_e32 v5, v1, v2
	s_nop 0
	v_cndmask_b32_e32 v3, v3, v6, vcc
	v_cndmask_b32_e32 v1, v1, v5, vcc
	v_add_u32_e32 v5, 1, v3
	v_cmp_ge_u32_e32 vcc, v1, v2
	s_nop 1
	v_cndmask_b32_e32 v1, v3, v5, vcc
	v_mad_u64_u32 v[2:3], s[2:3], v2, v1, v[2:3]
	v_cmp_ne_u32_e32 vcc, v4, v2
	v_mov_b32_e32 v20, 0
	s_cbranch_vccnz .Lxbar0_nl
	buffer_inv sc1
	buffer_wbl2 sc1
	s_waitcnt vmcnt(0)
	s_sub_u32 s2, s23, s34
	s_lshr_b32 s2, s2, 6
	s_add_u32 s6, s34, 0x2400
	s_addc_u32 s7, s35, 0
	s_add_u32 s6, s6, s2
	s_addc_u32 s7, s7, 0
	global_atomic_add v20, v10, s[6:7]
	s_branch .Lxbar0_poll

; __device__ __forceinline__ unsigned xb_ld(unsigned* p)              { return __hip_atomic_load(p, __ATOMIC_RELAXED, __HIP_MEMORY_SCOPE_AGENT); }
; __device__ __forceinline__ unsigned xb_add(unsigned* p, unsigned v) { return __hip_atomic_fetch_add(p, v, __ATOMIC_RELAXED, __HIP_MEMORY_SCOPE_AGENT); }
; #define XB_SPIN(cond, bar) do { unsigned _sp = 0; while (cond) { __builtin_amdgcn_s_sleep(1); \
;     if ((++_sp & 255u) == 0u) { if (xb_ld(&(bar)[XB_TMO])) break; if (_sp > XB_SPIN_CAP) { atomicAdd(&(bar)[XB_TMO], 1u); break; } } } } while (0)
; __device__ __forceinline__ void xcd_barrier(const XcdBarrier& b) {
;     ...
;             else XB_SPIN(xb_ld(&bar[XB_TOPGEN]) == tg, bar);
;             __builtin_amdgcn_fence(__ATOMIC_ACQUIRE, "agent");
;             xb_add(&bar[XB_XGEN(b.x)], one_);
;             asm volatile("s_waitcnt vmcnt(0)" ::: "memory");
;         } else {
;             XB_SPIN(xb_ld(&bar[XB_XGEN(b.x)]) == gen, bar);
;             __builtin_amdgcn_fence(__ATOMIC_ACQUIRE, "agent");
.Lxbar0_poll:
	s_add_u32 s6, s34, 0x2400
	s_addc_u32 s7, s35, 0
	v_add_u32_e32 v1, 1, v1
	v_mul_lo_u32 v1, v1, v0
	s_mov_b32 s2, 0

; __device__ __forceinline__ unsigned xb_ld(unsigned* p)              { return __hip_atomic_load(p, __ATOMIC_RELAXED, __HIP_MEMORY_SCOPE_AGENT); }
; __device__ __forceinline__ unsigned xb_add(unsigned* p, unsigned v) { return __hip_atomic_fetch_add(p, v, __ATOMIC_RELAXED, __HIP_MEMORY_SCOPE_AGENT); }
; #define XB_SPIN(cond, bar) do { unsigned _sp = 0; while (cond) { __builtin_amdgcn_s_sleep(1); \
;     if ((++_sp & 255u) == 0u) { if (xb_ld(&(bar)[XB_TMO])) break; if (_sp > XB_SPIN_CAP) { atomicAdd(&(bar)[XB_TMO], 1u); break; } } } } while (0)
; __device__ __forceinline__ void xcd_barrier(const XcdBarrier& b) {
;     ...
;         unsigned nloc = b.st[0], nx = b.st[1];
;         if (nloc == 0u) { xcd_barrier_complete(bar, b.x, nloc, nx); b.st[0] = nloc; b.st[1] = nx; }
;         const unsigned old = xb_add(&bar[XB_XSUB(b.x)], one_);
;         const unsigned gen = old / nloc;
;         if (old + 1u == (gen + 1u) * nloc) {
;             __builtin_amdgcn_fence(__ATOMIC_RELEASE, "agent");
;             asm volatile("s_waitcnt vmcnt(0)" ::: "memory");
;             const unsigned og = xb_add(&bar[XB_TOP], one_);
;             const unsigned tg = og / nx;
;             if (og + 1u == (tg + 1u) * nx) xb_add(&bar[XB_TOPGEN], one_);
;             else XB_SPIN(xb_ld(&bar[XB_TOPGEN]) == tg, bar);
;             __builtin_amdgcn_fence(__ATOMIC_ACQUIRE, "agent");
;             xb_add(&bar[XB_XGEN(b.x)], one_);
;             asm volatile("s_waitcnt vmcnt(0)" ::: "memory");
;         } else {
;             XB_SPIN(xb_ld(&bar[XB_XGEN(b.x)]) == gen, bar);
;             __builtin_amdgcn_fence(__ATOMIC_ACQUIRE, "agent");
;             asm volatile("s_waitcnt vmcnt(0)" ::: "memory");
;         }
.LBB0_430:
	v_readlane_b32 s4, v253, 57
	s_lshl_b32 s4, s4, 2
	s_add_u32 s25, s2, s4
	s_addc_u32 s24, s3, 0
	v_mov_b32_e32 v3, s25
	v_add_co_u32_e32 v6, vcc, 0x1000, v3
	v_mov_b32_e32 v3, s24
	s_nop 0
	v_addc_co_u32_e32 v7, vcc, 0, v3, vcc
	flat_atomic_add v5, v[6:7], v1 offset:1024 sc0
	v_cvt_f32_u32_e32 v3, v4
	v_sub_u32_e32 v6, 0, v4
	v_rcp_iflag_f32_e32 v3, v3
	s_nop 0
	v_mul_f32_e32 v3, 0x4f7ffffe, v3
	v_cvt_u32_f32_e32 v3, v3
	v_mul_lo_u32 v6, v6, v3
	v_mul_hi_u32 v6, v3, v6
	v_add_u32_e32 v3, v3, v6
	s_waitcnt vmcnt(0) lgkmcnt(0)
	v_mul_hi_u32 v3, v5, v3
	v_mul_lo_u32 v6, v3, v4
	v_sub_u32_e32 v6, v5, v6
	v_cmp_ge_u32_e32 vcc, v6, v4
	v_add_u32_e32 v7, 1, v3
	s_nop 0
	v_cndmask_b32_e32 v3, v3, v7, vcc
	v_sub_u32_e32 v7, v6, v4
	v_cndmask_b32_e32 v6, v6, v7, vcc
	v_cmp_ge_u32_e32 vcc, v6, v4
	v_add_u32_e32 v6, 1, v3
	s_nop 0
	v_cndmask_b32_e32 v3, v3, v6, vcc
	v_add_u32_e32 v6, 1, v5
	v_mad_u64_u32 v[4:5], s[4:5], v4, v3, v[4:5]
	v_cmp_ne_u32_e32 vcc, v6, v4
	v_mov_b32_e32 v20, 0
	s_cbranch_vccnz .Lxbar1_nl
	buffer_inv sc1
	buffer_wbl2 sc1
	s_waitcnt vmcnt(0)
	s_sub_u32 s4, s25, s2
	s_lshr_b32 s4, s4, 6
	s_add_u32 s8, s2, 0x2400
	s_addc_u32 s9, s3, 0
	s_add_u32 s8, s8, s4
	s_addc_u32 s9, s9, 0
	global_atomic_add v20, v1, s[8:9]
	s_branch .Lxbar1_poll

; __device__ __forceinline__ unsigned xb_ld(unsigned* p)              { return __hip_atomic_load(p, __ATOMIC_RELAXED, __HIP_MEMORY_SCOPE_AGENT); }
; __device__ __forceinline__ unsigned xb_add(unsigned* p, unsigned v) { return __hip_atomic_fetch_add(p, v, __ATOMIC_RELAXED, __HIP_MEMORY_SCOPE_AGENT); }
; #define XB_SPIN(cond, bar) do { unsigned _sp = 0; while (cond) { __builtin_amdgcn_s_sleep(1); \
;     if ((++_sp & 255u) == 0u) { if (xb_ld(&(bar)[XB_TMO])) break; if (_sp > XB_SPIN_CAP) { atomicAdd(&(bar)[XB_TMO], 1u); break; } } } } while (0)
; __device__ __forceinline__ void xcd_barrier(const XcdBarrier& b) {
;     ...
;             else XB_SPIN(xb_ld(&bar[XB_TOPGEN]) == tg, bar);
;             __builtin_amdgcn_fence(__ATOMIC_ACQUIRE, "agent");
;             xb_add(&bar[XB_XGEN(b.x)], one_);
;             asm volatile("s_waitcnt vmcnt(0)" ::: "memory");
;         } else {
;             XB_SPIN(xb_ld(&bar[XB_XGEN(b.x)]) == gen, bar);
;             __builtin_amdgcn_fence(__ATOMIC_ACQUIRE, "agent");
.Lxbar1_poll:
	s_add_u32 s8, s2, 0x2400
	s_addc_u32 s9, s3, 0
	v_add_u32_e32 v3, 1, v3
	v_mul_lo_u32 v3, v3, v0
	s_mov_b32 s4, 0

; __device__ __forceinline__ unsigned xb_ld(unsigned* p)              { return __hip_atomic_load(p, __ATOMIC_RELAXED, __HIP_MEMORY_SCOPE_AGENT); }
; __device__ __forceinline__ unsigned xb_add(unsigned* p, unsigned v) { return __hip_atomic_fetch_add(p, v, __ATOMIC_RELAXED, __HIP_MEMORY_SCOPE_AGENT); }
; #define XB_SPIN(cond, bar) do { unsigned _sp = 0; while (cond) { __builtin_amdgcn_s_sleep(1); \
;     if ((++_sp & 255u) == 0u) { if (xb_ld(&(bar)[XB_TMO])) break; if (_sp > XB_SPIN_CAP) { atomicAdd(&(bar)[XB_TMO], 1u); break; } } } } while (0)
; __device__ __forceinline__ void xcd_barrier(const XcdBarrier& b) {
;     ...
;         unsigned nloc = b.st[0], nx = b.st[1];
;         if (nloc == 0u) { xcd_barrier_complete(bar, b.x, nloc, nx); b.st[0] = nloc; b.st[1] = nx; }
;         const unsigned old = xb_add(&bar[XB_XSUB(b.x)], one_);
;         const unsigned gen = old / nloc;
;         if (old + 1u == (gen + 1u) * nloc) {
;             __builtin_amdgcn_fence(__ATOMIC_RELEASE, "agent");
;             asm volatile("s_waitcnt vmcnt(0)" ::: "memory");
;             const unsigned og = xb_add(&bar[XB_TOP], one_);
;             const unsigned tg = og / nx;
;             if (og + 1u == (tg + 1u) * nx) xb_add(&bar[XB_TOPGEN], one_);
;             else XB_SPIN(xb_ld(&bar[XB_TOPGEN]) == tg, bar);
;             __builtin_amdgcn_fence(__ATOMIC_ACQUIRE, "agent");
;             xb_add(&bar[XB_XGEN(b.x)], one_);
;             asm volatile("s_waitcnt vmcnt(0)" ::: "memory");
;         } else {
;             XB_SPIN(xb_ld(&bar[XB_XGEN(b.x)]) == gen, bar);
;             __builtin_amdgcn_fence(__ATOMIC_ACQUIRE, "agent");
;             asm volatile("s_waitcnt vmcnt(0)" ::: "memory");
;         }
.LBB0_681:
	v_readlane_b32 s6, v253, 57
	s_lshl_b32 s6, s6, 2
	s_add_u32 s27, s4, s6
	s_addc_u32 s26, s5, 0
	v_mov_b32_e32 v3, s27
	v_add_co_u32_e32 v6, vcc, 0x1000, v3
	v_mov_b32_e32 v3, s26
	s_nop 0
	v_addc_co_u32_e32 v7, vcc, 0, v3, vcc
	flat_atomic_add v5, v[6:7], v1 offset:1024 sc0
	v_cvt_f32_u32_e32 v3, v4
	v_sub_u32_e32 v6, 0, v4
	v_rcp_iflag_f32_e32 v3, v3
	s_nop 0
	v_mul_f32_e32 v3, 0x4f7ffffe, v3
	v_cvt_u32_f32_e32 v3, v3
	v_mul_lo_u32 v6, v6, v3
	v_mul_hi_u32 v6, v3, v6
	v_add_u32_e32 v3, v3, v6
	s_waitcnt vmcnt(0) lgkmcnt(0)
	v_mul_hi_u32 v3, v5, v3
	v_mul_lo_u32 v6, v3, v4
	v_sub_u32_e32 v6, v5, v6
	v_cmp_ge_u32_e32 vcc, v6, v4
	v_add_u32_e32 v7, 1, v3
	s_nop 0
	v_cndmask_b32_e32 v3, v3, v7, vcc
	v_sub_u32_e32 v7, v6, v4
	v_cndmask_b32_e32 v6, v6, v7, vcc
	v_cmp_ge_u32_e32 vcc, v6, v4
	v_add_u32_e32 v6, 1, v3
	s_nop 0
	v_cndmask_b32_e32 v3, v3, v6, vcc
	v_add_u32_e32 v6, 1, v5
	v_mad_u64_u32 v[4:5], s[6:7], v4, v3, v[4:5]
	v_cmp_ne_u32_e32 vcc, v6, v4
	v_mov_b32_e32 v20, 0
	s_cbranch_vccnz .Lxbar2_nl
	buffer_inv sc1
	buffer_wbl2 sc1
	s_waitcnt vmcnt(0)
	s_sub_u32 s6, s27, s4
	s_lshr_b32 s6, s6, 6
	s_add_u32 s10, s4, 0x2400
	s_addc_u32 s11, s5, 0
	s_add_u32 s10, s10, s6
	s_addc_u32 s11, s11, 0
	global_atomic_add v20, v1, s[10:11]
	s_branch .Lxbar2_poll

; __device__ __forceinline__ unsigned xb_ld(unsigned* p)              { return __hip_atomic_load(p, __ATOMIC_RELAXED, __HIP_MEMORY_SCOPE_AGENT); }
; __device__ __forceinline__ unsigned xb_add(unsigned* p, unsigned v) { return __hip_atomic_fetch_add(p, v, __ATOMIC_RELAXED, __HIP_MEMORY_SCOPE_AGENT); }
; #define XB_SPIN(cond, bar) do { unsigned _sp = 0; while (cond) { __builtin_amdgcn_s_sleep(1); \
;     if ((++_sp & 255u) == 0u) { if (xb_ld(&(bar)[XB_TMO])) break; if (_sp > XB_SPIN_CAP) { atomicAdd(&(bar)[XB_TMO], 1u); break; } } } } while (0)
; __device__ __forceinline__ void xcd_barrier(const XcdBarrier& b) {
;     ...
;             else XB_SPIN(xb_ld(&bar[XB_TOPGEN]) == tg, bar);
;             __builtin_amdgcn_fence(__ATOMIC_ACQUIRE, "agent");
;             xb_add(&bar[XB_XGEN(b.x)], one_);
;             asm volatile("s_waitcnt vmcnt(0)" ::: "memory");
;         } else {
;             XB_SPIN(xb_ld(&bar[XB_XGEN(b.x)]) == gen, bar);
;             __builtin_amdgcn_fence(__ATOMIC_ACQUIRE, "agent");
.Lxbar2_poll:
	s_add_u32 s10, s4, 0x2400
	s_addc_u32 s11, s5, 0
	v_add_u32_e32 v3, 1, v3
	v_mul_lo_u32 v3, v3, v0
	s_mov_b32 s6, 0

; __device__ __forceinline__ unsigned xb_ld(unsigned* p)              { return __hip_atomic_load(p, __ATOMIC_RELAXED, __HIP_MEMORY_SCOPE_AGENT); }
; __device__ __forceinline__ unsigned xb_add(unsigned* p, unsigned v) { return __hip_atomic_fetch_add(p, v, __ATOMIC_RELAXED, __HIP_MEMORY_SCOPE_AGENT); }
; #define XB_SPIN(cond, bar) do { unsigned _sp = 0; while (cond) { __builtin_amdgcn_s_sleep(1); \
;     if ((++_sp & 255u) == 0u) { if (xb_ld(&(bar)[XB_TMO])) break; if (_sp > XB_SPIN_CAP) { atomicAdd(&(bar)[XB_TMO], 1u); break; } } } } while (0)
; __device__ __forceinline__ void xcd_barrier(const XcdBarrier& b) {
;     ...
;         unsigned nloc = b.st[0], nx = b.st[1];
;         if (nloc == 0u) { xcd_barrier_complete(bar, b.x, nloc, nx); b.st[0] = nloc; b.st[1] = nx; }
;         const unsigned old = xb_add(&bar[XB_XSUB(b.x)], one_);
;         const unsigned gen = old / nloc;
;         if (old + 1u == (gen + 1u) * nloc) {
;             __builtin_amdgcn_fence(__ATOMIC_RELEASE, "agent");
;             asm volatile("s_waitcnt vmcnt(0)" ::: "memory");
;             const unsigned og = xb_add(&bar[XB_TOP], one_);
;             const unsigned tg = og / nx;
;             if (og + 1u == (tg + 1u) * nx) xb_add(&bar[XB_TOPGEN], one_);
;             else XB_SPIN(xb_ld(&bar[XB_TOPGEN]) == tg, bar);
;             __builtin_amdgcn_fence(__ATOMIC_ACQUIRE, "agent");
;             xb_add(&bar[XB_XGEN(b.x)], one_);
.LBB0_928:
	v_readlane_b32 s6, v253, 57
	s_lshl_b32 s6, s6, 2
	s_add_u32 s29, s4, s6
	s_addc_u32 s28, s5, 0
	v_mov_b32_e32 v3, s29
	v_add_co_u32_e32 v6, vcc, 0x1000, v3
	v_mov_b32_e32 v3, s28
	s_nop 0
	v_addc_co_u32_e32 v7, vcc, 0, v3, vcc
	flat_atomic_add v5, v[6:7], v1 offset:1024 sc0
	v_cvt_f32_u32_e32 v3, v4
	v_sub_u32_e32 v6, 0, v4
	v_rcp_iflag_f32_e32 v3, v3
	s_nop 0
	v_mul_f32_e32 v3, 0x4f7ffffe, v3
	v_cvt_u32_f32_e32 v3, v3
	v_mul_lo_u32 v6, v6, v3
	v_mul_hi_u32 v6, v3, v6
	v_add_u32_e32 v3, v3, v6
	s_waitcnt vmcnt(0) lgkmcnt(0)
	v_mul_hi_u32 v3, v5, v3
	v_mul_lo_u32 v6, v3, v4
	v_sub_u32_e32 v6, v5, v6
	v_cmp_ge_u32_e32 vcc, v6, v4
	v_add_u32_e32 v7, 1, v3
	s_nop 0
	v_cndmask_b32_e32 v3, v3, v7, vcc
	v_sub_u32_e32 v7, v6, v4
	v_cndmask_b32_e32 v6, v6, v7, vcc
	v_cmp_ge_u32_e32 vcc, v6, v4
	v_add_u32_e32 v6, 1, v3
	s_nop 0
	v_cndmask_b32_e32 v3, v3, v6, vcc
	v_add_u32_e32 v6, 1, v5
	v_mad_u64_u32 v[4:5], s[6:7], v4, v3, v[4:5]
	v_cmp_ne_u32_e32 vcc, v6, v4
	v_mov_b32_e32 v20, 0
	s_cbranch_vccnz .Lxbar4_nl
	buffer_inv sc1
	buffer_wbl2 sc1
	s_waitcnt vmcnt(0)
	s_sub_u32 s6, s29, s4
	s_lshr_b32 s6, s6, 6
	s_add_u32 s10, s4, 0x2400
	s_addc_u32 s11, s5, 0
	s_add_u32 s10, s10, s6
	s_addc_u32 s11, s11, 0
	global_atomic_add v20, v1, s[10:11]
	s_branch .Lxbar4_poll

; __device__ __forceinline__ unsigned xb_ld(unsigned* p)              { return __hip_atomic_load(p, __ATOMIC_RELAXED, __HIP_MEMORY_SCOPE_AGENT); }
; __device__ __forceinline__ unsigned xb_add(unsigned* p, unsigned v) { return __hip_atomic_fetch_add(p, v, __ATOMIC_RELAXED, __HIP_MEMORY_SCOPE_AGENT); }
; #define XB_SPIN(cond, bar) do { unsigned _sp = 0; while (cond) { __builtin_amdgcn_s_sleep(1); \
;     if ((++_sp & 255u) == 0u) { if (xb_ld(&(bar)[XB_TMO])) break; if (_sp > XB_SPIN_CAP) { atomicAdd(&(bar)[XB_TMO], 1u); break; } } } } while (0)
; __device__ __forceinline__ void xcd_barrier(const XcdBarrier& b) {
;     ...
;         unsigned nloc = b.st[0], nx = b.st[1];
;         if (nloc == 0u) { xcd_barrier_complete(bar, b.x, nloc, nx); b.st[0] = nloc; b.st[1] = nx; }
;         const unsigned old = xb_add(&bar[XB_XSUB(b.x)], one_);
;         const unsigned gen = old / nloc;
;         if (old + 1u == (gen + 1u) * nloc) {
;             __builtin_amdgcn_fence(__ATOMIC_RELEASE, "agent");
;             asm volatile("s_waitcnt vmcnt(0)" ::: "memory");
;             const unsigned og = xb_add(&bar[XB_TOP], one_);
;             const unsigned tg = og / nx;
;             if (og + 1u == (tg + 1u) * nx) xb_add(&bar[XB_TOPGEN], one_);
;             else XB_SPIN(xb_ld(&bar[XB_TOPGEN]) == tg, bar);
;             __builtin_amdgcn_fence(__ATOMIC_ACQUIRE, "agent");
;             xb_add(&bar[XB_XGEN(b.x)], one_);
.LBB0_1016:
	v_readlane_b32 s4, v253, 57
	s_lshl_b32 s4, s4, 2
	s_add_u32 s27, s2, s4
	s_addc_u32 s26, s3, 0
	v_mov_b32_e32 v3, s27
	v_add_co_u32_e32 v6, vcc, 0x1000, v3
	v_mov_b32_e32 v3, s26
	s_nop 0
	v_addc_co_u32_e32 v7, vcc, 0, v3, vcc
	flat_atomic_add v5, v[6:7], v1 offset:1024 sc0
	v_cvt_f32_u32_e32 v3, v4
	v_sub_u32_e32 v6, 0, v4
	v_rcp_iflag_f32_e32 v3, v3
	s_nop 0
	v_mul_f32_e32 v3, 0x4f7ffffe, v3
	v_cvt_u32_f32_e32 v3, v3
	v_mul_lo_u32 v6, v6, v3
	v_mul_hi_u32 v6, v3, v6
	v_add_u32_e32 v3, v3, v6
	s_waitcnt vmcnt(0) lgkmcnt(0)
	v_mul_hi_u32 v3, v5, v3
	v_mul_lo_u32 v6, v3, v4
	v_sub_u32_e32 v6, v5, v6
	v_cmp_ge_u32_e32 vcc, v6, v4
	v_add_u32_e32 v7, 1, v3
	s_nop 0
	v_cndmask_b32_e32 v3, v3, v7, vcc
	v_sub_u32_e32 v7, v6, v4
	v_cndmask_b32_e32 v6, v6, v7, vcc
	v_cmp_ge_u32_e32 vcc, v6, v4
	v_add_u32_e32 v6, 1, v3
	s_nop 0
	v_cndmask_b32_e32 v3, v3, v6, vcc
	v_add_u32_e32 v6, 1, v5
	v_mad_u64_u32 v[4:5], s[4:5], v4, v3, v[4:5]
	v_cmp_ne_u32_e32 vcc, v6, v4
	v_mov_b32_e32 v20, 0
	s_cbranch_vccnz .Lxbar5_nl
	buffer_inv sc1
	buffer_wbl2 sc1
	s_waitcnt vmcnt(0)
	s_sub_u32 s4, s27, s2
	s_lshr_b32 s4, s4, 6
	s_add_u32 s8, s2, 0x2400
	s_addc_u32 s9, s3, 0
	s_add_u32 s8, s8, s4
	s_addc_u32 s9, s9, 0
	global_atomic_add v20, v1, s[8:9]
	s_branch .Lxbar5_poll
